# blocked fp8 expert-weight layout + sc0 sc1 (write-through) on P0's expert stores
# speedup vs baseline: 1.0197x; 1.0172x over previous
; #define MOE_LOAD(v, it) do { _Pragma("unroll") for (int i_ = 0; i_ < 64; ++i_) v[i_] = __builtin_nontemporal_load((it).src + (size_t)(2 * i_) * (it).stride); } while (0)
;     ...
;         for (int j = 0; j < nmine; j += 2) {
;             const int it1 = gw + (j + 1) * NGW, it2 = gw + (j + 2) * NGW;
;             ib = moe_item(wg, wu, wd, win, wout, wpn, wpd, F.ws, it1 <= last ? it1 : last, F.lane); MOE_LOAD(vb, ib);
;             MOE_PROC(va, ia);
;             ia = moe_item(wg, wu, wd, win, wout, wpn, wpd, F.ws, it2 <= last ? it2 : last, F.lane); MOE_LOAD(va, ia);
;             MOE_PROC(vb, ib);
.LBB0_80:
	s_lshl_b64 s[68:69], s[68:69], 3
	v_lshl_add_u64 v[14:15], v[16:17], 0, s[68:69]
	global_load_dword v87, v[16:17], off nt
	v_lshl_add_u64 v[16:17], v[14:15], 0, s[68:69]
	v_lshl_add_u64 v[30:31], v[16:17], 0, s[68:69]
	v_lshl_add_u64 v[32:33], v[30:31], 0, s[68:69]
	v_lshl_add_u64 v[34:35], v[32:33], 0, s[68:69]
	v_lshl_add_u64 v[36:37], v[34:35], 0, s[68:69]
	v_lshl_add_u64 v[38:39], v[36:37], 0, s[68:69]
	v_lshl_add_u64 v[40:41], v[38:39], 0, s[68:69]
	global_load_dword v92, v[14:15], off nt
	global_load_dword v91, v[16:17], off nt
	global_load_dword v90, v[30:31], off nt
	global_load_dword v89, v[32:33], off nt
	global_load_dword v88, v[34:35], off nt
	global_load_dword v86, v[36:37], off nt
	global_load_dword v85, v[38:39], off nt
	global_load_dword v83, v[40:41], off nt
	v_lshl_add_u64 v[14:15], v[40:41], 0, s[68:69]
	v_lshl_add_u64 v[16:17], v[14:15], 0, s[68:69]
	global_load_dword v84, v[14:15], off nt
	global_load_dword v79, v[16:17], off nt
	v_lshl_add_u64 v[14:15], v[16:17], 0, s[68:69]
	global_load_dword v80, v[14:15], off nt
	v_lshl_add_u64 v[14:15], v[14:15], 0, s[68:69]
	global_load_dword v75, v[14:15], off nt
	v_lshl_add_u64 v[14:15], v[14:15], 0, s[68:69]
	global_load_dword v76, v[14:15], off nt
	v_lshl_add_u64 v[14:15], v[14:15], 0, s[68:69]
	global_load_dword v71, v[14:15], off nt
	v_lshl_add_u64 v[14:15], v[14:15], 0, s[68:69]
	global_load_dword v72, v[14:15], off nt
	v_lshl_add_u64 v[14:15], v[14:15], 0, s[68:69]
	global_load_dword v65, v[14:15], off nt
	v_lshl_add_u64 v[14:15], v[14:15], 0, s[68:69]
	global_load_dword v66, v[14:15], off nt
	v_lshl_add_u64 v[14:15], v[14:15], 0, s[68:69]
	global_load_dword v61, v[14:15], off nt
	v_lshl_add_u64 v[14:15], v[14:15], 0, s[68:69]
	global_load_dword v62, v[14:15], off nt
	v_lshl_add_u64 v[14:15], v[14:15], 0, s[68:69]
	global_load_dword v57, v[14:15], off nt
	v_lshl_add_u64 v[14:15], v[14:15], 0, s[68:69]
	global_load_dword v58, v[14:15], off nt
	v_lshl_add_u64 v[14:15], v[14:15], 0, s[68:69]
	global_load_dword v53, v[14:15], off nt
	v_lshl_add_u64 v[14:15], v[14:15], 0, s[68:69]
	global_load_dword v54, v[14:15], off nt
	v_lshl_add_u64 v[14:15], v[14:15], 0, s[68:69]
	global_load_dword v45, v[14:15], off nt
	v_lshl_add_u64 v[14:15], v[14:15], 0, s[68:69]
	global_load_dword v46, v[14:15], off nt
	v_lshl_add_u64 v[14:15], v[14:15], 0, s[68:69]
	global_load_dword v35, v[14:15], off nt
	v_lshl_add_u64 v[14:15], v[14:15], 0, s[68:69]
	global_load_dword v36, v[14:15], off nt
	v_lshl_add_u64 v[14:15], v[14:15], 0, s[68:69]
	global_load_dword v33, v[14:15], off nt
	v_lshl_add_u64 v[14:15], v[14:15], 0, s[68:69]
	global_load_dword v34, v[14:15], off nt
	v_lshl_add_u64 v[14:15], v[14:15], 0, s[68:69]
	global_load_dword v31, v[14:15], off nt
	v_lshl_add_u64 v[14:15], v[14:15], 0, s[68:69]
	global_load_dword v32, v[14:15], off nt
	v_lshl_add_u64 v[14:15], v[14:15], 0, s[68:69]
	global_load_dword v29, v[14:15], off nt
	v_lshl_add_u64 v[14:15], v[14:15], 0, s[68:69]
	global_load_dword v30, v[14:15], off nt
	v_lshl_add_u64 v[14:15], v[14:15], 0, s[68:69]
	global_load_dword v81, v[14:15], off nt
	v_lshl_add_u64 v[14:15], v[14:15], 0, s[68:69]
	global_load_dword v82, v[14:15], off nt
	v_lshl_add_u64 v[14:15], v[14:15], 0, s[68:69]
	global_load_dword v77, v[14:15], off nt
	v_lshl_add_u64 v[14:15], v[14:15], 0, s[68:69]
	global_load_dword v78, v[14:15], off nt
	v_lshl_add_u64 v[14:15], v[14:15], 0, s[68:69]
	global_load_dword v73, v[14:15], off nt
	v_lshl_add_u64 v[14:15], v[14:15], 0, s[68:69]
	global_load_dword v74, v[14:15], off nt
	v_lshl_add_u64 v[14:15], v[14:15], 0, s[68:69]
	global_load_dword v69, v[14:15], off nt
	v_lshl_add_u64 v[14:15], v[14:15], 0, s[68:69]
	global_load_dword v70, v[14:15], off nt
	v_lshl_add_u64 v[14:15], v[14:15], 0, s[68:69]
	global_load_dword v67, v[14:15], off nt
	v_lshl_add_u64 v[14:15], v[14:15], 0, s[68:69]
	global_load_dword v68, v[14:15], off nt
	v_lshl_add_u64 v[14:15], v[14:15], 0, s[68:69]
	global_load_dword v63, v[14:15], off nt
	v_lshl_add_u64 v[14:15], v[14:15], 0, s[68:69]
	global_load_dword v64, v[14:15], off nt
	v_lshl_add_u64 v[14:15], v[14:15], 0, s[68:69]
	global_load_dword v59, v[14:15], off nt
	v_lshl_add_u64 v[14:15], v[14:15], 0, s[68:69]
	global_load_dword v60, v[14:15], off nt
	v_lshl_add_u64 v[14:15], v[14:15], 0, s[68:69]
	global_load_dword v55, v[14:15], off nt
	v_lshl_add_u64 v[14:15], v[14:15], 0, s[68:69]
	global_load_dword v56, v[14:15], off nt
	v_lshl_add_u64 v[14:15], v[14:15], 0, s[68:69]
	global_load_dword v51, v[14:15], off nt
	v_lshl_add_u64 v[14:15], v[14:15], 0, s[68:69]
	global_load_dword v52, v[14:15], off nt
	v_lshl_add_u64 v[14:15], v[14:15], 0, s[68:69]
	global_load_dword v38, v[14:15], off nt
	v_lshl_add_u64 v[14:15], v[14:15], 0, s[68:69]
	global_load_dword v39, v[14:15], off nt
	v_lshl_add_u64 v[14:15], v[14:15], 0, s[68:69]
	global_load_dword v40, v[14:15], off nt
	v_lshl_add_u64 v[14:15], v[14:15], 0, s[68:69]
	global_load_dword v42, v[14:15], off nt
	v_lshl_add_u64 v[14:15], v[14:15], 0, s[68:69]
	global_load_dword v37, v[14:15], off nt
	v_lshl_add_u64 v[14:15], v[14:15], 0, s[68:69]
	global_load_dword v41, v[14:15], off nt
	v_lshl_add_u64 v[14:15], v[14:15], 0, s[68:69]
	global_load_dword v43, v[14:15], off nt
	v_lshl_add_u64 v[14:15], v[14:15], 0, s[68:69]
	global_load_dword v44, v[14:15], off nt
	v_lshl_add_u64 v[14:15], v[14:15], 0, s[68:69]
	global_load_dword v47, v[14:15], off nt
	v_lshl_add_u64 v[14:15], v[14:15], 0, s[68:69]
	global_load_dword v48, v[14:15], off nt
	v_lshl_add_u64 v[14:15], v[14:15], 0, s[68:69]
	global_load_dword v49, v[14:15], off nt
	v_lshl_add_u64 v[14:15], v[14:15], 0, s[68:69]
	s_waitcnt vmcnt(62)
	ds_write2st64_b32 v28, v93, v101 offset1:1
	ds_write2st64_b32 v28, v99, v100 offset0:2 offset1:3
	ds_write2st64_b32 v28, v97, v98 offset0:4 offset1:5
	ds_write2st64_b32 v28, v95, v96 offset0:6 offset1:7
	ds_write2st64_b32 v21, v94, v124 offset0:8 offset1:9
	ds_write2st64_b32 v21, v104, v114 offset0:10 offset1:11
	ds_write2st64_b32 v21, v105, v115 offset0:12 offset1:13
	ds_write2st64_b32 v21, v106, v116 offset0:14 offset1:15
	ds_write2st64_b32 v22, v107, v117 offset0:16 offset1:17
	ds_write2st64_b32 v22, v108, v118 offset0:18 offset1:19
	ds_write2st64_b32 v22, v109, v119 offset0:20 offset1:21
	ds_write2st64_b32 v22, v110, v120 offset0:22 offset1:23
	ds_write2st64_b32 v23, v111, v121 offset0:24 offset1:25
	ds_write2st64_b32 v23, v112, v122 offset0:26 offset1:27
	global_load_dword v50, v[14:15], off nt
	ds_write2st64_b32 v23, v102, v103 offset0:28 offset1:29
	ds_write2st64_b32 v23, v113, v123 offset0:30 offset1:31
	ds_write2st64_b32 v24, v125, v126 offset0:32 offset1:33
	ds_write2st64_b32 v24, v127, v128 offset0:34 offset1:35
	ds_write2st64_b32 v24, v129, v130 offset0:36 offset1:37
	ds_write2st64_b32 v24, v131, v132 offset0:38 offset1:39
	ds_write2st64_b32 v25, v133, v134 offset0:40 offset1:41
	ds_write2st64_b32 v25, v135, v136 offset0:42 offset1:43
	ds_write2st64_b32 v25, v137, v138 offset0:44 offset1:45
	ds_write2st64_b32 v25, v139, v140 offset0:46 offset1:47
	ds_write2st64_b32 v26, v141, v142 offset0:48 offset1:49
	ds_write2st64_b32 v26, v143, v144 offset0:50 offset1:51
	ds_write2st64_b32 v26, v146, v147 offset0:52 offset1:53
	ds_write2st64_b32 v26, v148, v149 offset0:54 offset1:55
	ds_write2st64_b32 v27, v151, v152 offset0:56 offset1:57
	ds_write2st64_b32 v27, v153, v154 offset0:58 offset1:59
	ds_write2st64_b32 v27, v155, v157 offset0:60 offset1:61
	ds_write2st64_b32 v27, v158, v159 offset0:62 offset1:63
	s_waitcnt lgkmcnt(0)
	ds_read2_b32 v[16:17], v1 offset1:32
	v_lshlrev_b64 v[14:15], s44, v[2:3]
	v_lshl_add_u64 v[12:13], v[12:13], 0, v[14:15]
	v_lshl_add_u64 v[98:99], v[12:13], 0, v[6:7]
	v_mov_b32_e32 v12, 0
	s_waitcnt lgkmcnt(0)
	v_mul_f32_e32 v4, 0x42800000, v16
	v_mul_f32_e32 v13, 0x42800000, v17
	ds_read2_b32 v[16:17], v1 offset0:64 offset1:96
	ds_read2_b32 v[94:95], v1 offset0:128 offset1:160
	v_cvt_pk_fp8_f32 v12, v4, v13
	v_lshlrev_b64 v[14:15], s46, v[2:3]
	v_lshl_add_u64 v[10:11], v[10:11], 0, v[14:15]
	s_waitcnt lgkmcnt(1)
	v_mul_f32_e32 v4, 0x42800000, v16
	v_mul_f32_e32 v13, 0x42800000, v17
	v_cvt_pk_fp8_f32 v12, v4, v13 op_sel:[0,0,1]
	s_waitcnt lgkmcnt(0)
	v_mul_f32_e32 v4, 0x42800000, v94
	ds_read2_b32 v[14:15], v1 offset0:192 offset1:224
	v_mul_f32_e32 v16, 0x42800000, v95
	v_mov_b32_e32 v13, 0
	v_cvt_pk_fp8_f32 v13, v4, v16
	ds_read2_b32 v[16:17], v145 offset1:32
	s_waitcnt lgkmcnt(1)
	v_mul_f32_e32 v4, 0x42800000, v14
	v_mul_f32_e32 v93, 0x42800000, v15
	ds_read2_b32 v[14:15], v145 offset0:64 offset1:96
	v_cvt_pk_fp8_f32 v13, v4, v93 op_sel:[0,0,1]
	s_waitcnt lgkmcnt(1)
	v_mul_f32_e32 v4, 0x42800000, v16
	v_mul_f32_e32 v93, 0x42800000, v17
	ds_read2_b32 v[16:17], v145 offset0:128 offset1:160
	s_waitcnt lgkmcnt(1)
	v_mul_f32_e32 v96, 0x42800000, v14
	v_mov_b32_e32 v14, 0
	v_cvt_pk_fp8_f32 v14, v4, v93
	v_mul_f32_e32 v97, 0x42800000, v15
	s_waitcnt lgkmcnt(0)
	v_mul_f32_e32 v4, 0x42800000, v16
	v_mul_f32_e32 v93, 0x42800000, v17
	ds_read2_b32 v[16:17], v145 offset0:192 offset1:224
	v_mov_b32_e32 v15, 0
	v_cvt_pk_fp8_f32 v15, v4, v93
	ds_read2_b32 v[94:95], v9 offset1:32
	v_cvt_pk_fp8_f32 v14, v96, v97 op_sel:[0,0,1]
	s_waitcnt lgkmcnt(1)
	v_mul_f32_e32 v4, 0x42800000, v16
	v_mul_f32_e32 v16, 0x42800000, v17
	v_cvt_pk_fp8_f32 v15, v4, v16 op_sel:[0,0,1]
	ds_read2_b32 v[16:17], v9 offset0:64 offset1:96
	s_waitcnt lgkmcnt(1)
	v_mul_f32_e32 v4, 0x42800000, v94
	v_mul_f32_e32 v93, 0x42800000, v95
	v_mov_b32_e32 v94, 0
	ds_read2_b32 v[96:97], v9 offset0:128 offset1:160
	v_cvt_pk_fp8_f32 v94, v4, v93
	global_store_dwordx4 v[98:99], v[12:15], off sc0 sc1
	s_waitcnt lgkmcnt(1)
	v_mul_f32_e32 v4, 0x42800000, v16
	v_mov_b32_e32 v95, 0
	v_mul_f32_e32 v12, 0x42800000, v17
	v_cvt_pk_fp8_f32 v94, v4, v12 op_sel:[0,0,1]
	s_waitcnt lgkmcnt(0)
	v_mul_f32_e32 v4, 0x42800000, v96
	ds_read2_b32 v[12:13], v9 offset0:192 offset1:224
	v_mul_f32_e32 v14, 0x42800000, v97
	v_cvt_pk_fp8_f32 v95, v4, v14
	ds_read2_b32 v[14:15], v150 offset1:32
	v_mov_b32_e32 v96, 0
	s_waitcnt lgkmcnt(1)
; #define MOE_LOAD(v, it) do { _Pragma("unroll") for (int i_ = 0; i_ < 64; ++i_) v[i_] = __builtin_nontemporal_load((it).src + (size_t)(2 * i_) * (it).stride); } while (0)
;     ...
;         for (int j = 0; j < nmine; j += 2) {
;             const int it1 = gw + (j + 1) * NGW, it2 = gw + (j + 2) * NGW;
;             ib = moe_item(wg, wu, wd, win, wout, wpn, wpd, F.ws, it1 <= last ? it1 : last, F.lane); MOE_LOAD(vb, ib);
;             MOE_PROC(va, ia);
;             ia = moe_item(wg, wu, wd, win, wout, wpn, wpd, F.ws, it2 <= last ? it2 : last, F.lane); MOE_LOAD(va, ia);
;             MOE_PROC(vb, ib);
;         }
	v_mul_f32_e32 v4, 0x42800000, v12
	v_mul_f32_e32 v16, 0x42800000, v13
	ds_read2_b32 v[12:13], v150 offset0:64 offset1:96
	v_cvt_pk_fp8_f32 v95, v4, v16 op_sel:[0,0,1]
	s_waitcnt lgkmcnt(1)
	v_mul_f32_e32 v4, 0x42800000, v14
	v_mul_f32_e32 v16, 0x42800000, v15
	ds_read2_b32 v[14:15], v150 offset0:128 offset1:160
	s_waitcnt lgkmcnt(1)
	v_mul_f32_e32 v17, 0x42800000, v12
	v_mul_f32_e32 v93, 0x42800000, v13
	ds_read2_b32 v[12:13], v150 offset0:192 offset1:224
	v_cvt_pk_fp8_f32 v96, v4, v16
	s_waitcnt lgkmcnt(1)
	v_mul_f32_e32 v4, 0x42800000, v14
	v_mul_f32_e32 v14, 0x42800000, v15
	v_mov_b32_e32 v97, 0
	v_cvt_pk_fp8_f32 v97, v4, v14
	s_waitcnt lgkmcnt(0)
	v_mul_f32_e32 v4, 0x42800000, v12
	v_mul_f32_e32 v12, 0x42800000, v13
	v_cvt_pk_fp8_f32 v96, v17, v93 op_sel:[0,0,1]
	v_cvt_pk_fp8_f32 v97, v4, v12 op_sel:[0,0,1]
	s_lshl_b32 s4, s42, 3
	ds_read2_b32 v[12:13], v18 offset1:32
	v_lshl_add_u64 v[16:17], v[98:99], 0, s[4:5]
	ds_read2_b32 v[14:15], v18 offset0:64 offset1:96
	global_store_dwordx4 v[16:17], v[94:97], off sc0 sc1
	ds_read2_b32 v[94:95], v18 offset0:128 offset1:160
	s_waitcnt lgkmcnt(2)
	v_mul_f32_e32 v4, 0x42800000, v12
	v_mul_f32_e32 v13, 0x42800000, v13
	v_mov_b32_e32 v12, 0
	s_waitcnt lgkmcnt(1)
	v_mul_f32_e32 v93, 0x42800000, v14
	v_mul_f32_e32 v96, 0x42800000, v15
	v_cvt_pk_fp8_f32 v12, v4, v13
	s_waitcnt lgkmcnt(0)
	v_mul_f32_e32 v4, 0x42800000, v94
	v_mul_f32_e32 v94, 0x42800000, v95
	ds_read2_b32 v[14:15], v18 offset0:192 offset1:224
	v_mov_b32_e32 v13, 0
	v_cvt_pk_fp8_f32 v13, v4, v94
	ds_read2_b32 v[94:95], v156 offset1:32
	v_cvt_pk_fp8_f32 v12, v93, v96 op_sel:[0,0,1]
	s_waitcnt lgkmcnt(1)
	v_mul_f32_e32 v4, 0x42800000, v14
	v_mul_f32_e32 v14, 0x42800000, v15
	ds_read2_b32 v[96:97], v156 offset0:64 offset1:96
	v_cvt_pk_fp8_f32 v13, v4, v14 op_sel:[0,0,1]
	s_waitcnt lgkmcnt(1)
	v_mul_f32_e32 v4, 0x42800000, v94
	v_mul_f32_e32 v15, 0x42800000, v95
	v_mov_b32_e32 v14, 0
	ds_read2_b32 v[94:95], v156 offset0:128 offset1:160
	v_cvt_pk_fp8_f32 v14, v4, v15
	s_waitcnt lgkmcnt(1)
	v_mul_f32_e32 v4, 0x42800000, v96
	v_mul_f32_e32 v15, 0x42800000, v97
	ds_read2_b32 v[96:97], v156 offset0:192 offset1:224
	v_cvt_pk_fp8_f32 v14, v4, v15 op_sel:[0,0,1]
	s_waitcnt lgkmcnt(1)
	v_mul_f32_e32 v4, 0x42800000, v94
	v_mul_f32_e32 v93, 0x42800000, v95
	ds_read2_b32 v[94:95], v19 offset1:32
	s_waitcnt lgkmcnt(1)
	v_mul_f32_e32 v100, 0x42800000, v96
	v_mul_f32_e32 v101, 0x42800000, v97
	v_mov_b32_e32 v15, 0
	ds_read2_b32 v[96:97], v19 offset0:64 offset1:96
	v_cvt_pk_fp8_f32 v15, v4, v93
	s_waitcnt lgkmcnt(1)
	v_mul_f32_e32 v4, 0x42800000, v94
	v_mul_f32_e32 v93, 0x42800000, v95
	v_mov_b32_e32 v94, 0
	ds_read2_b32 v[98:99], v19 offset0:128 offset1:160
	v_cvt_pk_fp8_f32 v94, v4, v93
	s_waitcnt lgkmcnt(1)
	v_mul_f32_e32 v4, 0x42800000, v96
	v_mul_f32_e32 v93, 0x42800000, v97
	ds_read2_b32 v[96:97], v19 offset0:192 offset1:224
	v_cvt_pk_fp8_f32 v94, v4, v93 op_sel:[0,0,1]
	s_waitcnt lgkmcnt(1)
	v_mul_f32_e32 v4, 0x42800000, v98
	v_mul_f32_e32 v93, 0x42800000, v99
	v_mov_b32_e32 v95, 0
	ds_read2_b32 v[98:99], v160 offset1:32
	v_cvt_pk_fp8_f32 v95, v4, v93
	s_waitcnt lgkmcnt(1)
	v_mul_f32_e32 v4, 0x42800000, v96
	v_mul_f32_e32 v93, 0x42800000, v97
	ds_read2_b32 v[96:97], v160 offset0:64 offset1:96
	v_cvt_pk_fp8_f32 v95, v4, v93 op_sel:[0,0,1]
	s_waitcnt lgkmcnt(1)
	v_mul_f32_e32 v4, 0x42800000, v98
	v_mul_f32_e32 v93, 0x42800000, v99
	ds_read2_b32 v[98:99], v160 offset0:128 offset1:160
	v_cvt_pk_fp8_f32 v15, v100, v101 op_sel:[0,0,1]
	s_waitcnt lgkmcnt(1)
	v_mul_f32_e32 v102, 0x42800000, v96
	v_mov_b32_e32 v96, 0
	ds_read2_b32 v[100:101], v160 offset0:192 offset1:224
	v_mul_f32_e32 v103, 0x42800000, v97
	v_cvt_pk_fp8_f32 v96, v4, v93
	s_waitcnt lgkmcnt(1)
	v_mul_f32_e32 v4, 0x42800000, v98
	v_mul_f32_e32 v93, 0x42800000, v99
	v_mov_b32_e32 v97, 0
	v_cvt_pk_fp8_f32 v97, v4, v93
	s_waitcnt lgkmcnt(0)
	v_mul_f32_e32 v4, 0x42800000, v100
	v_mul_f32_e32 v93, 0x42800000, v101
	v_cvt_pk_fp8_f32 v96, v102, v103 op_sel:[0,0,1]
	v_cvt_pk_fp8_f32 v97, v4, v93 op_sel:[0,0,1]
	v_lshl_add_u64 v[16:17], v[16:17], 0, s[4:5]
	global_store_dwordx4 v[16:17], v[12:15], off sc0 sc1
	s_add_i32 s91, s91, 2
	s_cmp_ge_i32 s91, s6
	v_lshl_add_u64 v[12:13], v[16:17], 0, s[4:5]
	global_store_dwordx4 v[12:13], v[94:97], off sc0 sc1
	s_waitcnt lgkmcnt(0)
	s_cbranch_scc1 .LBB0_130

.LBB0_105:
	s_lshl_b64 s[46:47], s[46:47], 3
	global_load_dword v93, v[16:17], off nt
	v_lshl_add_u64 v[16:17], v[16:17], 0, s[46:47]
	v_lshl_add_u64 v[94:95], v[16:17], 0, s[46:47]
	v_lshl_add_u64 v[96:97], v[94:95], 0, s[46:47]
	v_lshl_add_u64 v[102:103], v[96:97], 0, s[46:47]
	v_lshl_add_u64 v[104:105], v[102:103], 0, s[46:47]
	v_lshl_add_u64 v[106:107], v[104:105], 0, s[46:47]
	v_lshl_add_u64 v[108:109], v[106:107], 0, s[46:47]
	v_lshl_add_u64 v[110:111], v[108:109], 0, s[46:47]
	global_load_dword v101, v[16:17], off nt
	global_load_dword v99, v[94:95], off nt
	global_load_dword v100, v[96:97], off nt
	s_nop 0
	global_load_dword v97, v[102:103], off nt
	global_load_dword v98, v[104:105], off nt
	global_load_dword v95, v[106:107], off nt
	global_load_dword v96, v[108:109], off nt
	global_load_dword v94, v[110:111], off nt
	v_lshl_add_u64 v[16:17], v[110:111], 0, s[46:47]
	s_waitcnt vmcnt(9)
	ds_write2st64_b32 v28, v87, v92 offset1:1
	v_lshl_add_u64 v[102:103], v[16:17], 0, s[46:47]
	global_load_dword v124, v[16:17], off nt
	global_load_dword v104, v[102:103], off nt
	v_lshl_add_u64 v[16:17], v[102:103], 0, s[46:47]
	global_load_dword v114, v[16:17], off nt
	v_lshl_add_u64 v[16:17], v[16:17], 0, s[46:47]
	global_load_dword v105, v[16:17], off nt
	v_lshl_add_u64 v[16:17], v[16:17], 0, s[46:47]
	global_load_dword v115, v[16:17], off nt
	v_lshl_add_u64 v[16:17], v[16:17], 0, s[46:47]
	global_load_dword v106, v[16:17], off nt
	v_lshl_add_u64 v[16:17], v[16:17], 0, s[46:47]
	global_load_dword v116, v[16:17], off nt
	v_lshl_add_u64 v[16:17], v[16:17], 0, s[46:47]
	global_load_dword v107, v[16:17], off nt
	v_lshl_add_u64 v[16:17], v[16:17], 0, s[46:47]
	global_load_dword v117, v[16:17], off nt
	v_lshl_add_u64 v[16:17], v[16:17], 0, s[46:47]
	global_load_dword v108, v[16:17], off nt
	v_lshl_add_u64 v[16:17], v[16:17], 0, s[46:47]
	global_load_dword v118, v[16:17], off nt
	v_lshl_add_u64 v[16:17], v[16:17], 0, s[46:47]
	global_load_dword v109, v[16:17], off nt
	v_lshl_add_u64 v[16:17], v[16:17], 0, s[46:47]
	global_load_dword v119, v[16:17], off nt
	v_lshl_add_u64 v[16:17], v[16:17], 0, s[46:47]
	global_load_dword v110, v[16:17], off nt
	v_lshl_add_u64 v[16:17], v[16:17], 0, s[46:47]
	global_load_dword v120, v[16:17], off nt
	v_lshl_add_u64 v[16:17], v[16:17], 0, s[46:47]
	global_load_dword v111, v[16:17], off nt
	v_lshl_add_u64 v[16:17], v[16:17], 0, s[46:47]
	global_load_dword v121, v[16:17], off nt
	v_lshl_add_u64 v[16:17], v[16:17], 0, s[46:47]
	global_load_dword v112, v[16:17], off nt
	v_lshl_add_u64 v[16:17], v[16:17], 0, s[46:47]
	global_load_dword v122, v[16:17], off nt
	v_lshl_add_u64 v[16:17], v[16:17], 0, s[46:47]
	global_load_dword v102, v[16:17], off nt
	v_lshl_add_u64 v[16:17], v[16:17], 0, s[46:47]
	global_load_dword v103, v[16:17], off nt
	v_lshl_add_u64 v[16:17], v[16:17], 0, s[46:47]
	global_load_dword v113, v[16:17], off nt
	v_lshl_add_u64 v[16:17], v[16:17], 0, s[46:47]
	global_load_dword v123, v[16:17], off nt
	v_lshl_add_u64 v[16:17], v[16:17], 0, s[46:47]
	global_load_dword v125, v[16:17], off nt
	v_lshl_add_u64 v[16:17], v[16:17], 0, s[46:47]
	global_load_dword v126, v[16:17], off nt
	v_lshl_add_u64 v[16:17], v[16:17], 0, s[46:47]
	global_load_dword v127, v[16:17], off nt
	v_lshl_add_u64 v[16:17], v[16:17], 0, s[46:47]
	global_load_dword v128, v[16:17], off nt
	v_lshl_add_u64 v[16:17], v[16:17], 0, s[46:47]
	global_load_dword v129, v[16:17], off nt
	v_lshl_add_u64 v[16:17], v[16:17], 0, s[46:47]
	global_load_dword v130, v[16:17], off nt
	v_lshl_add_u64 v[16:17], v[16:17], 0, s[46:47]
	global_load_dword v131, v[16:17], off nt
	v_lshl_add_u64 v[16:17], v[16:17], 0, s[46:47]
	global_load_dword v132, v[16:17], off nt
	v_lshl_add_u64 v[16:17], v[16:17], 0, s[46:47]
	global_load_dword v133, v[16:17], off nt
	v_lshl_add_u64 v[16:17], v[16:17], 0, s[46:47]
	global_load_dword v134, v[16:17], off nt
	v_lshl_add_u64 v[16:17], v[16:17], 0, s[46:47]
	global_load_dword v135, v[16:17], off nt
	v_lshl_add_u64 v[16:17], v[16:17], 0, s[46:47]
	global_load_dword v136, v[16:17], off nt
	v_lshl_add_u64 v[16:17], v[16:17], 0, s[46:47]
	global_load_dword v137, v[16:17], off nt
	v_lshl_add_u64 v[16:17], v[16:17], 0, s[46:47]
	global_load_dword v138, v[16:17], off nt
	v_lshl_add_u64 v[16:17], v[16:17], 0, s[46:47]
	global_load_dword v139, v[16:17], off nt
	v_lshl_add_u64 v[16:17], v[16:17], 0, s[46:47]
	global_load_dword v140, v[16:17], off nt
	v_lshl_add_u64 v[16:17], v[16:17], 0, s[46:47]
	global_load_dword v141, v[16:17], off nt
	v_lshl_add_u64 v[16:17], v[16:17], 0, s[46:47]
	global_load_dword v142, v[16:17], off nt
	v_lshl_add_u64 v[16:17], v[16:17], 0, s[46:47]
	global_load_dword v143, v[16:17], off nt
	v_lshl_add_u64 v[16:17], v[16:17], 0, s[46:47]
	global_load_dword v144, v[16:17], off nt
	v_lshl_add_u64 v[16:17], v[16:17], 0, s[46:47]
	global_load_dword v146, v[16:17], off nt
	v_lshl_add_u64 v[16:17], v[16:17], 0, s[46:47]
	global_load_dword v147, v[16:17], off nt
	v_lshl_add_u64 v[16:17], v[16:17], 0, s[46:47]
	global_load_dword v148, v[16:17], off nt
	v_lshl_add_u64 v[16:17], v[16:17], 0, s[46:47]
	global_load_dword v149, v[16:17], off nt
	v_lshl_add_u64 v[16:17], v[16:17], 0, s[46:47]
	global_load_dword v151, v[16:17], off nt
	v_lshl_add_u64 v[16:17], v[16:17], 0, s[46:47]
	global_load_dword v152, v[16:17], off nt
	v_lshl_add_u64 v[16:17], v[16:17], 0, s[46:47]
	global_load_dword v153, v[16:17], off nt
	v_lshl_add_u64 v[16:17], v[16:17], 0, s[46:47]
	global_load_dword v154, v[16:17], off nt
	v_lshl_add_u64 v[16:17], v[16:17], 0, s[46:47]
	global_load_dword v155, v[16:17], off nt
	v_lshl_add_u64 v[16:17], v[16:17], 0, s[46:47]
	global_load_dword v157, v[16:17], off nt
	v_lshl_add_u64 v[16:17], v[16:17], 0, s[46:47]
	global_load_dword v158, v[16:17], off nt
	v_lshl_add_u64 v[16:17], v[16:17], 0, s[46:47]
	ds_write2st64_b32 v28, v91, v90 offset0:2 offset1:3
	ds_write2st64_b32 v28, v89, v88 offset0:4 offset1:5
	ds_write2st64_b32 v28, v86, v85 offset0:6 offset1:7
	ds_write2st64_b32 v21, v83, v84 offset0:8 offset1:9
	ds_write2st64_b32 v21, v79, v80 offset0:10 offset1:11
	ds_write2st64_b32 v21, v75, v76 offset0:12 offset1:13
	ds_write2st64_b32 v21, v71, v72 offset0:14 offset1:15
	ds_write2st64_b32 v22, v65, v66 offset0:16 offset1:17
	ds_write2st64_b32 v22, v61, v62 offset0:18 offset1:19
	ds_write2st64_b32 v22, v57, v58 offset0:20 offset1:21
	ds_write2st64_b32 v22, v53, v54 offset0:22 offset1:23
	ds_write2st64_b32 v23, v45, v46 offset0:24 offset1:25
	ds_write2st64_b32 v23, v35, v36 offset0:26 offset1:27
	ds_write2st64_b32 v23, v33, v34 offset0:28 offset1:29
	ds_write2st64_b32 v23, v31, v32 offset0:30 offset1:31
	ds_write2st64_b32 v24, v29, v30 offset0:32 offset1:33
	ds_write2st64_b32 v24, v81, v82 offset0:34 offset1:35
	ds_write2st64_b32 v24, v77, v78 offset0:36 offset1:37
	ds_write2st64_b32 v24, v73, v74 offset0:38 offset1:39
	ds_write2st64_b32 v25, v69, v70 offset0:40 offset1:41
	ds_write2st64_b32 v25, v67, v68 offset0:42 offset1:43
	ds_write2st64_b32 v25, v63, v64 offset0:44 offset1:45
	ds_write2st64_b32 v25, v59, v60 offset0:46 offset1:47
	ds_write2st64_b32 v26, v55, v56 offset0:48 offset1:49
	ds_write2st64_b32 v26, v51, v52 offset0:50 offset1:51
	global_load_dword v159, v[16:17], off nt
	ds_write2st64_b32 v26, v38, v39 offset0:52 offset1:53
	ds_write2st64_b32 v26, v40, v42 offset0:54 offset1:55
	ds_write2st64_b32 v27, v37, v41 offset0:56 offset1:57
	ds_write2st64_b32 v27, v43, v44 offset0:58 offset1:59
	ds_write2st64_b32 v27, v47, v48 offset0:60 offset1:61
	ds_write2st64_b32 v27, v49, v50 offset0:62 offset1:63
	s_waitcnt lgkmcnt(0)
	ds_read2_b32 v[16:17], v1 offset1:32
	v_mov_b32_e32 v30, 0
	ds_read2_b32 v[32:33], v1 offset0:128 offset1:160
	v_mov_b32_e32 v31, 0
	v_add_u32_e32 v145, 0x400, v1
	s_waitcnt lgkmcnt(1)
	v_mul_f32_e32 v4, 0x42800000, v16
	v_mul_f32_e32 v15, 0x42800000, v17
	ds_read2_b32 v[16:17], v1 offset0:64 offset1:96
	v_cvt_pk_fp8_f32 v30, v4, v15
	ds_read2_b32 v[34:35], v145 offset0:128 offset1:160
	v_add_u32_e32 v150, 0x400, v9
	ds_read2_b32 v[38:39], v150 offset0:128 offset1:160
	s_waitcnt lgkmcnt(2)
	v_mul_f32_e32 v4, 0x42800000, v16
	v_mul_f32_e32 v15, 0x42800000, v17
	ds_read2_b32 v[16:17], v1 offset0:192 offset1:224
	v_cvt_pk_fp8_f32 v30, v4, v15 op_sel:[0,0,1]
	v_mul_f32_e32 v4, 0x42800000, v32
	v_mul_f32_e32 v15, 0x42800000, v33
	v_cvt_pk_fp8_f32 v31, v4, v15
	s_waitcnt lgkmcnt(0)
	v_mul_f32_e32 v4, 0x42800000, v16
	v_mul_f32_e32 v15, 0x42800000, v17
	ds_read2_b32 v[16:17], v145 offset0:64 offset1:96
	ds_read2_b32 v[32:33], v145 offset1:32
	v_cvt_pk_fp8_f32 v31, v4, v15 op_sel:[0,0,1]
	v_lshl_add_u64 v[10:11], v[10:11], 0, v[6:7]
	v_add_u32_e32 v156, 0x400, v18
	s_waitcnt lgkmcnt(1)
	v_mul_f32_e32 v29, 0x42800000, v16
	v_mul_f32_e32 v36, 0x42800000, v17
	ds_read2_b32 v[16:17], v145 offset0:192 offset1:224
	s_waitcnt lgkmcnt(1)
	v_mul_f32_e32 v4, 0x42800000, v32
	v_mul_f32_e32 v15, 0x42800000, v33
	v_mov_b32_e32 v32, 0
	v_cvt_pk_fp8_f32 v32, v4, v15
	v_mul_f32_e32 v4, 0x42800000, v34
	v_mul_f32_e32 v15, 0x42800000, v35
	v_mov_b32_e32 v33, 0
	ds_read2_b32 v[34:35], v9 offset1:32
	v_cvt_pk_fp8_f32 v33, v4, v15
	s_waitcnt lgkmcnt(1)
	v_mul_f32_e32 v4, 0x42800000, v16
	v_mul_f32_e32 v15, 0x42800000, v17
	ds_read2_b32 v[16:17], v9 offset0:64 offset1:96
	v_cvt_pk_fp8_f32 v32, v29, v36 op_sel:[0,0,1]
	ds_read2_b32 v[36:37], v9 offset0:128 offset1:160
	v_cvt_pk_fp8_f32 v33, v4, v15 op_sel:[0,0,1]
	s_waitcnt lgkmcnt(2)
	v_mul_f32_e32 v4, 0x42800000, v34
	v_mul_f32_e32 v15, 0x42800000, v35
	v_mov_b32_e32 v34, 0
	v_cvt_pk_fp8_f32 v34, v4, v15
	s_waitcnt lgkmcnt(1)
	v_mul_f32_e32 v4, 0x42800000, v16
	v_mul_f32_e32 v15, 0x42800000, v17
	ds_read2_b32 v[16:17], v9 offset0:192 offset1:224
	s_waitcnt lgkmcnt(1)
	v_mul_f32_e32 v29, 0x42800000, v36
	v_mul_f32_e32 v36, 0x42800000, v37
	v_mov_b32_e32 v35, 0
	v_cvt_pk_fp8_f32 v35, v29, v36
	ds_read2_b32 v[36:37], v150 offset1:32
	v_cvt_pk_fp8_f32 v34, v4, v15 op_sel:[0,0,1]
	s_waitcnt lgkmcnt(1)
	v_mul_f32_e32 v4, 0x42800000, v16
	v_mul_f32_e32 v15, 0x42800000, v17
	ds_read2_b32 v[16:17], v150 offset0:64 offset1:96
	v_cvt_pk_fp8_f32 v35, v4, v15 op_sel:[0,0,1]
	s_waitcnt lgkmcnt(1)
	v_mul_f32_e32 v4, 0x42800000, v36
	v_mul_f32_e32 v15, 0x42800000, v37
	v_mov_b32_e32 v36, 0
	v_cvt_pk_fp8_f32 v36, v4, v15
	s_waitcnt lgkmcnt(0)
	v_mul_f32_e32 v4, 0x42800000, v16
	v_mul_f32_e32 v15, 0x42800000, v17
	ds_read2_b32 v[16:17], v150 offset0:192 offset1:224
	v_cvt_pk_fp8_f32 v36, v4, v15 op_sel:[0,0,1]
	v_mul_f32_e32 v4, 0x42800000, v38
	v_mul_f32_e32 v15, 0x42800000, v39
	v_mov_b32_e32 v37, 0
	v_cvt_pk_fp8_f32 v37, v4, v15
	s_waitcnt lgkmcnt(0)
; __device__ __forceinline__ MoeItem moe_item(const float* wg, const float* wu, const float* wd, const float* win, const float* wout, const float* wpn, const float* wpd, unsigned char* ws, int r, int lane) {
;     ...
;     const int mat = r / MOE_IE, q = r % MOE_IE, e = mat / 3, which = mat % 3, kb = q / 64, nb = q % 64, n0 = nb * 32;
;     const float* src = (which == 0 ? wg : (which == 1 ? wu : wd)) + (size_t)e * DM * DFF + (size_t)(kb * 128 + (lane >> 5)) * DFF + n0 + (lane & 31);
;     unsigned char* dst;
;     if (which < 2) dst = ws + WS_WGUT + ((size_t)(e * 16 + (n0 >> 7)) * 256 + which * 128 + (n0 & 127)) * DM;
;     else dst = ws + WS_WDT + ((size_t)e * DM + n0) * DFF;
;     MoeItem it; it.stride = DFF; it.dpitch = DM; it.src = src; it.dst = dst + kb * 128 + (size_t)(lane >> 3) * DM + 16 * (lane & 7); return it;
	v_mul_f32_e32 v4, 0x42800000, v16
	v_mul_f32_e32 v15, 0x42800000, v17
	ds_read2_b32 v[16:17], v18 offset1:32
	v_cvt_pk_fp8_f32 v37, v4, v15 op_sel:[0,0,1]
	global_store_dwordx4 v[10:11], v[30:33], off sc0 sc1
	ds_read2_b32 v[32:33], v18 offset0:64 offset1:96
	s_lshl_b64 s[38:39], s[38:39], 3
	s_waitcnt lgkmcnt(1)
	v_mul_f32_e32 v4, 0x42800000, v16
	v_mul_f32_e32 v15, 0x42800000, v17
	ds_read2_b32 v[16:17], v18 offset0:128 offset1:160
	v_mov_b32_e32 v30, 0
	v_cvt_pk_fp8_f32 v30, v4, v15
	s_waitcnt lgkmcnt(1)
	v_mul_f32_e32 v4, 0x42800000, v32
	v_mov_b32_e32 v31, 0
	s_waitcnt lgkmcnt(0)
	v_mul_f32_e32 v29, 0x42800000, v16
	v_mul_f32_e32 v32, 0x42800000, v17
	ds_read2_b32 v[16:17], v18 offset0:192 offset1:224
	v_mul_f32_e32 v15, 0x42800000, v33
	v_cvt_pk_fp8_f32 v31, v29, v32
	ds_read2_b32 v[32:33], v156 offset1:32
	v_cvt_pk_fp8_f32 v30, v4, v15 op_sel:[0,0,1]
	s_waitcnt lgkmcnt(1)
	v_mul_f32_e32 v4, 0x42800000, v16
	v_mul_f32_e32 v15, 0x42800000, v17
	ds_read2_b32 v[16:17], v156 offset0:64 offset1:96
	v_lshl_add_u64 v[10:11], v[10:11], 0, s[38:39]
	global_store_dwordx4 v[10:11], v[34:37], off sc0 sc1
	ds_read2_b32 v[34:35], v156 offset0:128 offset1:160
	v_cvt_pk_fp8_f32 v31, v4, v15 op_sel:[0,0,1]
	s_waitcnt lgkmcnt(2)
	v_mul_f32_e32 v4, 0x42800000, v32
	v_mul_f32_e32 v15, 0x42800000, v33
	v_mov_b32_e32 v32, 0
	v_cvt_pk_fp8_f32 v32, v4, v15
	s_waitcnt lgkmcnt(1)
	v_mul_f32_e32 v4, 0x42800000, v16
	v_mul_f32_e32 v15, 0x42800000, v17
	ds_read2_b32 v[16:17], v156 offset0:192 offset1:224
	s_waitcnt lgkmcnt(1)
	v_mul_f32_e32 v29, 0x42800000, v34
	v_mul_f32_e32 v34, 0x42800000, v35
	v_mov_b32_e32 v33, 0
	v_cvt_pk_fp8_f32 v33, v29, v34
	ds_read2_b32 v[34:35], v19 offset1:32
	v_cvt_pk_fp8_f32 v32, v4, v15 op_sel:[0,0,1]
	s_waitcnt lgkmcnt(1)
	v_mul_f32_e32 v4, 0x42800000, v16
	v_mul_f32_e32 v15, 0x42800000, v17
	ds_read2_b32 v[16:17], v19 offset0:64 offset1:96
	ds_read2_b32 v[36:37], v19 offset0:128 offset1:160
	v_cvt_pk_fp8_f32 v33, v4, v15 op_sel:[0,0,1]
	s_waitcnt lgkmcnt(2)
	v_mul_f32_e32 v4, 0x42800000, v34
	v_mul_f32_e32 v15, 0x42800000, v35
	v_mov_b32_e32 v34, 0
	v_cvt_pk_fp8_f32 v34, v4, v15
	s_waitcnt lgkmcnt(1)
	v_mul_f32_e32 v4, 0x42800000, v16
	v_mul_f32_e32 v15, 0x42800000, v17
	ds_read2_b32 v[16:17], v19 offset0:192 offset1:224
	s_waitcnt lgkmcnt(1)
	v_mul_f32_e32 v29, 0x42800000, v36
	v_mul_f32_e32 v36, 0x42800000, v37
	v_mov_b32_e32 v35, 0
	v_add_u32_e32 v160, 0x400, v19
	v_cvt_pk_fp8_f32 v35, v29, v36
	ds_read2_b32 v[36:37], v160 offset1:32
	v_cvt_pk_fp8_f32 v34, v4, v15 op_sel:[0,0,1]
	s_waitcnt lgkmcnt(1)
	v_mul_f32_e32 v4, 0x42800000, v16
	v_mul_f32_e32 v15, 0x42800000, v17
	ds_read2_b32 v[16:17], v160 offset0:64 offset1:96
	ds_read2_b32 v[38:39], v160 offset0:128 offset1:160
	v_cvt_pk_fp8_f32 v35, v4, v15 op_sel:[0,0,1]
	s_waitcnt lgkmcnt(2)
	v_mul_f32_e32 v4, 0x42800000, v36
	v_mul_f32_e32 v15, 0x42800000, v37
	v_mov_b32_e32 v36, 0
	v_cvt_pk_fp8_f32 v36, v4, v15
	s_waitcnt lgkmcnt(1)
	v_mul_f32_e32 v4, 0x42800000, v16
	v_mul_f32_e32 v15, 0x42800000, v17
	ds_read2_b32 v[16:17], v160 offset0:192 offset1:224
	s_waitcnt lgkmcnt(1)
	v_mul_f32_e32 v29, 0x42800000, v38
	v_mul_f32_e32 v38, 0x42800000, v39
	v_mov_b32_e32 v37, 0
	v_cvt_pk_fp8_f32 v37, v29, v38
	v_cvt_pk_fp8_f32 v36, v4, v15 op_sel:[0,0,1]
	s_waitcnt lgkmcnt(0)
	v_mul_f32_e32 v4, 0x42800000, v16
	v_mul_f32_e32 v15, 0x42800000, v17
	v_cvt_pk_fp8_f32 v37, v4, v15 op_sel:[0,0,1]
	v_lshl_add_u64 v[10:11], v[10:11], 0, s[38:39]
	global_store_dwordx4 v[10:11], v[30:33], off sc0 sc1
	v_lshl_add_u64 v[10:11], v[10:11], 0, s[38:39]
	global_store_dwordx4 v[10:11], v[34:37], off sc0 sc1
	s_waitcnt lgkmcnt(0)
	s_add_i32 s3, s89, s3
	s_mov_b32 s96, 0
	s_min_i32 s43, s3, s7
	s_cmp_lt_i32 s43, 0x19000
	s_mov_b64 s[38:39], -1
	s_cbranch_scc0 .LBB0_126
	s_cmp_lt_i32 s43, 0x18c00
	s_cbranch_scc0 .LBB0_123
	s_cmp_lt_i32 s43, 0x18000
	s_cbranch_scc0 .LBB0_113
	s_mov_b32 s96, 1
	s_ashr_i32 s4, s43, 31
	s_lshr_b32 s4, s4, 22
	s_add_i32 s4, s43, s4
	s_ashr_i32 s39, s4, 10
	s_and_b32 s4, s4, 0xfc00
	s_sub_i32 s46, s43, s4
	s_mul_hi_i32 s4, s43, 0x2aaaaaab
	s_lshr_b32 s38, s4, 31
	s_ashr_i32 s4, s4, 9
	s_add_i32 s38, s4, s38
	s_mul_hi_i32 s4, s39, 0x55555556
	s_lshr_b32 s45, s4, 31
	s_add_i32 s4, s4, s45
	s_mul_i32 s4, s4, 3
	s_sub_i32 s4, s39, s4
	s_sext_i32_i16 s39, s46
	s_bfe_u32 s39, s39, 0x60019
	s_add_i32 s45, s46, s39
	s_and_b32 s39, s45, 0xffc0
	s_sub_i32 s39, s46, s39
	s_sext_i32_i16 s84, s39
	s_lshl_b32 s46, s84, 5
	s_ashr_i32 s39, s38, 31
	s_ashr_i32 s47, s46, 31
	s_cmp_gt_i32 s4, 1
	s_mov_b64 s[70:71], -1
	s_cbranch_scc0 .LBB0_110
	s_lshl_b64 s[68:69], s[38:39], 22
	s_lshl_b64 s[70:71], s[46:47], 11
	s_add_u32 s68, s73, s68
	s_addc_u32 s69, s74, s69
	s_add_u32 s68, s68, s70
	s_addc_u32 s69, s69, s71
	s_mov_b64 s[70:71], 0
